# RSTAT partial-sum loop: conservative vmcnt(0) between the first five partial loads removed (all five in flight together)
# speedup vs baseline: 1.0072x; 1.0072x over previous
; __device__ __forceinline__ void ret_stats(const float* PT, float* ST, int gtid, int nthr) {
;     for (int i = gtid; i < M * 8; i += nthr) { const int hd = i / M, row = i - hd * M; const f32x2_t* p = (const f32x2_t*)PT + (size_t)hd * 16 * M + row; float sv = 0.f, sq = 0.f;
; #pragma unroll
;         for (int k = 0; k < 16; ++k) { const f32x2_t v = p[(size_t)k * M]; sv += v.x; sq += v.y; }
;         *(f32x2_t*)(ST + ((size_t)row * 8 + hd) * 2) = (f32x2_t){sv, sq}; }
; }
.LBB0_32:
	v_ashrrev_i32_e32 v1, 31, v0
	v_lshrrev_b32_e32 v1, 17, v1
	v_add_u32_e32 v1, v0, v1
	v_ashrrev_i32_e32 v8, 15, v1
	v_and_b32_e32 v10, 0xffff8000, v1
	v_ashrrev_i32_e32 v9, 31, v8
	v_ashrrev_i32_e32 v11, 31, v10
	v_lshlrev_b64 v[12:13], 22, v[8:9]
	v_lshlrev_b64 v[14:15], 3, v[10:11]
	v_sub_co_u32_e32 v12, vcc, v12, v14
	s_mov_b32 s3, 0x1da00000
	s_nop 0
	v_subb_co_u32_e32 v13, vcc, v13, v15, vcc
	v_lshl_add_u64 v[14:15], v[4:5], 0, s[10:11]
	v_lshl_add_u64 v[12:13], v[14:15], 0, v[12:13]
	v_add_co_u32_e32 v14, vcc, s3, v12
	s_mov_b32 s3, 0x1da40000
	s_nop 0
	v_addc_co_u32_e32 v15, vcc, 0, v13, vcc
	v_add_co_u32_e32 v16, vcc, s3, v12
	global_load_dwordx2 v[14:15], v[14:15], off
	s_nop 0
	v_addc_co_u32_e32 v17, vcc, 0, v13, vcc
	s_mov_b32 s3, 0x1da80000
	global_load_dwordx2 v[16:17], v[16:17], off
	v_add_co_u32_e32 v18, vcc, s3, v12
	s_mov_b32 s3, 0x1dac0000
	s_nop 0
	v_addc_co_u32_e32 v19, vcc, 0, v13, vcc
	global_load_dwordx2 v[18:19], v[18:19], off
	v_add_co_u32_e32 v20, vcc, s3, v12
	s_mov_b32 s3, 0x1db00000
	s_nop 0
	v_addc_co_u32_e32 v21, vcc, 0, v13, vcc
	global_load_dwordx2 v[20:21], v[20:21], off
	v_add_co_u32_e32 v22, vcc, s3, v12
	s_mov_b32 s3, 0x1db40000
	s_nop 0
	v_addc_co_u32_e32 v23, vcc, 0, v13, vcc
	global_load_dwordx2 v[22:23], v[22:23], off
	v_lshlrev_b64 v[8:9], 3, v[8:9]
	v_lshlrev_b64 v[10:11], 6, v[10:11]
	v_add_u32_e32 v0, s2, v0
	v_lshl_add_u64 v[4:5], v[4:5], 0, s[4:5]
	s_waitcnt vmcnt(4)
	v_pk_add_f32 v[14:15], v[14:15], 0 op_sel_hi:[1,0]
	s_waitcnt vmcnt(3)
	v_pk_add_f32 v[14:15], v[14:15], v[16:17]
	v_add_co_u32_e32 v16, vcc, s3, v12
	s_mov_b32 s3, 0x1db80000
	s_nop 0
	v_addc_co_u32_e32 v17, vcc, 0, v13, vcc
	s_waitcnt vmcnt(2)
	v_pk_add_f32 v[14:15], v[14:15], v[18:19]
	v_add_co_u32_e32 v18, vcc, s3, v12
	s_mov_b32 s3, 0x1dbc0000
	s_nop 0
	v_addc_co_u32_e32 v19, vcc, 0, v13, vcc
	s_waitcnt vmcnt(1)
	v_pk_add_f32 v[14:15], v[14:15], v[20:21]
	v_add_co_u32_e32 v20, vcc, s3, v12
	s_mov_b32 s3, 0x1dc00000
	s_nop 0
	v_addc_co_u32_e32 v21, vcc, 0, v13, vcc
	s_waitcnt vmcnt(0)
	v_pk_add_f32 v[14:15], v[14:15], v[22:23]
	v_add_co_u32_e32 v22, vcc, s3, v12
	s_mov_b32 s3, 0x1dc40000
	s_nop 0
	v_addc_co_u32_e32 v23, vcc, 0, v13, vcc
	v_add_co_u32_e32 v24, vcc, s3, v12
	s_mov_b32 s3, 0x1dc80000
	s_nop 0
	v_addc_co_u32_e32 v25, vcc, 0, v13, vcc
	v_add_co_u32_e32 v26, vcc, s3, v12
	s_mov_b32 s3, 0x1dcc0000
	s_nop 0
	v_addc_co_u32_e32 v27, vcc, 0, v13, vcc
	global_load_dwordx2 v[16:17], v[16:17], off
	v_add_co_u32_e32 v28, vcc, s3, v12
	global_load_dwordx2 v[18:19], v[18:19], off
	s_nop 0
	v_addc_co_u32_e32 v29, vcc, 0, v13, vcc
	s_mov_b32 s3, 0x1dd00000
	global_load_dwordx2 v[20:21], v[20:21], off
	v_add_co_u32_e32 v30, vcc, s3, v12
	global_load_dwordx2 v[22:23], v[22:23], off
	s_nop 0
	v_addc_co_u32_e32 v31, vcc, 0, v13, vcc
	s_mov_b32 s3, 0x1dd40000
	global_load_dwordx2 v[24:25], v[24:25], off
	v_add_co_u32_e32 v32, vcc, s3, v12
	global_load_dwordx2 v[26:27], v[26:27], off
	s_nop 0
	v_addc_co_u32_e32 v33, vcc, 0, v13, vcc
	s_mov_b32 s3, 0x1dd80000
	global_load_dwordx2 v[28:29], v[28:29], off
	v_add_co_u32_e32 v34, vcc, s3, v12
	global_load_dwordx2 v[30:31], v[30:31], off
	s_nop 0
	v_addc_co_u32_e32 v35, vcc, 0, v13, vcc
	s_mov_b32 s3, 0x1ddc0000
	global_load_dwordx2 v[32:33], v[32:33], off
	v_add_co_u32_e32 v12, vcc, s3, v12
	global_load_dwordx2 v[34:35], v[34:35], off
	s_nop 0
	v_addc_co_u32_e32 v13, vcc, 0, v13, vcc
	global_load_dwordx2 v[12:13], v[12:13], off
	v_sub_co_u32_e32 v8, vcc, v8, v10
	s_mov_b32 s3, 0x3ffff
	s_nop 0
	v_subb_co_u32_e32 v9, vcc, v9, v11, vcc
	v_lshl_add_u64 v[10:11], v[6:7], 0, s[10:11]
	v_cmp_lt_i32_e32 vcc, s3, v0
	v_lshl_add_u64 v[8:9], v[10:11], 0, v[8:9]
	v_lshl_add_u64 v[6:7], v[6:7], 0, s[6:7]
	s_or_b64 s[8:9], vcc, s[8:9]
	s_waitcnt vmcnt(10)
	v_pk_add_f32 v[14:15], v[14:15], v[16:17]
	s_waitcnt vmcnt(9)
	v_pk_add_f32 v[14:15], v[14:15], v[18:19]
	s_waitcnt vmcnt(8)
	v_pk_add_f32 v[14:15], v[14:15], v[20:21]
	s_waitcnt vmcnt(7)
	v_pk_add_f32 v[14:15], v[14:15], v[22:23]
	s_waitcnt vmcnt(6)
	v_pk_add_f32 v[14:15], v[14:15], v[24:25]
	s_waitcnt vmcnt(5)
	v_pk_add_f32 v[14:15], v[14:15], v[26:27]
	s_waitcnt vmcnt(4)
	v_pk_add_f32 v[14:15], v[14:15], v[28:29]
	s_waitcnt vmcnt(3)
	v_pk_add_f32 v[14:15], v[14:15], v[30:31]
	s_waitcnt vmcnt(2)
	v_pk_add_f32 v[14:15], v[14:15], v[32:33]
	s_waitcnt vmcnt(1)
	v_pk_add_f32 v[14:15], v[14:15], v[34:35]
	s_waitcnt vmcnt(0)
	v_pk_add_f32 v[12:13], v[14:15], v[12:13]
	global_store_dwordx2 v[8:9], v[12:13], off
	s_andn2_b64 exec, exec, s[8:9]
	s_cbranch_execnz .LBB0_32
